# MLA loop: softmax row sums kept per lane-half in the loop, combined once at the loop exit
# speedup vs baseline: 1.0138x; 1.0029x over previous
; #define SBAR() __builtin_amdgcn_sched_barrier(0)
; #define ATT_PKN(P, BASE, OUT) do { u32x4 w = {cvt_pk_bf16(P[BASE + 0], P[BASE + 1]), cvt_pk_bf16(P[BASE + 2], P[BASE + 3]), cvt_pk_bf16(P[BASE + 4], P[BASE + 5]), cvt_pk_bf16(P[BASE + 6], P[BASE + 7])}; \
;     OUT = __builtin_bit_cast(bf16x8, w); } while (0)
; #define SLOAD(i, j) do { const int _row = KROW(j); skn[i] = *(const bf16x8*)(Knp + (size_t)(_row + sr) * ldk + c8 * 8); sv[i] = *(const bf16x8*)(Vp + (size_t)(_row + sr) * ldv + c8 * 8); \
;         if (krw) skr[i] = *(const bf16x8*)(Krp + (size_t)(_row + sr2) * 32 + c4 * 8); } while (0)
; #define SWRITEO(boff, i) do { *(LAS bf16x8*)(lds + (boff) + kn_st) = skn[i]; *(LAS bf16x8*)(lds + (boff) + v_stw) = sv[i]; if (krw) *(LAS bf16x8*)(lds + (boff) + kr_st) = skr[i]; } while (0)
; #define PVO(boff) do { pv_one<0>(o0, vb0 + (boff), pa0, pa1, pa2, pa3); pv_one<1>(o1, vb0 + (boff), pa0, pa1, pa2, pa3); } while (0)
; #define SWAIT() asm volatile("s_waitcnt vmcnt(2)" ::: "memory")
; __device__ __forceinline__ void finishSM(f32x16& p0, f32x16& p1, float alpha, float& l_reg, bf16x8& pa0, bf16x8& pa1, bf16x8& pa2, bf16x8& pa3) {
; #pragma unroll
;     for (int r = 0; r < 16; ++r) p1[r] = EXP_PROBE ? fmaf(p1[r], 0.001f, 1.f) : __builtin_amdgcn_exp2f(p1[r]);
;     float ps = 0.f;
; #pragma unroll
;     for (int r = 0; r < 16; ++r) ps += p0[r];
; #pragma unroll
;     for (int r = 0; r < 16; ++r) ps += p1[r];
;     { auto rr = __builtin_amdgcn_permlane32_swap(__float_as_uint(ps), __float_as_uint(ps), false, false);
;       ps = __uint_as_float(rr[0]) + __uint_as_float(rr[1]); }
;     l_reg = l_reg * alpha + ps;
;     ATT_PKN(p0, 0, pa0); ATT_PKN(p0, 8, pa1); ATT_PKN(p1, 0, pa2); ATT_PKN(p1, 8, pa3);
; }
; template <int DQK, bool FIXM> ...
;     ...
;         SBAR(); qkt<DQK>(pB0, pB1, lds + bK, qr, r32, hi, negm);
;         finishSM(pA0, pA1, alA, l_reg, pa0, pa1, pa2, pa3); SBAR();
;         SLOAD(1, j + 2); SBAR();
;         if constexpr (FIXM) pv_psm<true>(o0, o1, vb0 + bV, pa0, pa1, pa2, pa3, pB0, pB1, m_reg, negm, alB); else { PVO(bV); partialSM<false>(pB0, pB1, m_reg, negm, alB); }
;         SWAIT(); SWRITEO(bW, 0);
.LBB0_523:
	s_waitcnt lgkmcnt(0)
	s_barrier
	ds_read_b128 v[4:7], v209 offset:20480
	ds_read_b128 v[8:11], v209 offset:24576
	ds_read_b128 v[174:177], v210 offset:20480
	ds_read_b128 v[246:249], v210 offset:24576
	ds_read_b128 v[250:253], v211 offset:20480
	ds_read_b128 v[78:81], v211 offset:24576
	ds_read_b128 v[12:15], v212 offset:20480
	v_exp_f32_e32 v98, v98
	v_exp_f32_e32 v99, v99
	v_exp_f32_e32 v100, v100
	v_exp_f32_e32 v101, v101
	v_exp_f32_e32 v102, v102
	v_exp_f32_e32 v103, v103
	v_exp_f32_e32 v104, v104
	v_exp_f32_e32 v105, v105
	s_waitcnt lgkmcnt(6)
	v_mfma_f32_32x32x16_bf16 v[130:145], v[4:7], v[166:169], v[82:97]
	ds_read_b128 v[4:7], v212 offset:24576
	v_exp_f32_e32 v106, v106
	v_exp_f32_e32 v107, v107
	v_exp_f32_e32 v108, v108
	v_cvt_pk_bf16_f32 v74, v243, v245
	s_waitcnt lgkmcnt(6)
	v_mfma_f32_32x32x16_bf16 v[114:129], v[8:11], v[166:169], v[82:97]
	ds_read_b128 v[8:11], v219 offset:28672
	v_exp_f32_e32 v109, v109
	v_exp_f32_e32 v110, v110
	v_exp_f32_e32 v111, v111
	v_cvt_pk_bf16_f32 v75, v241, v244
	s_waitcnt lgkmcnt(6)
	v_mfma_f32_32x32x16_bf16 v[130:145], v[174:177], v[162:165], v[130:145]
	ds_read_b128 v[174:177], v219 offset:30720
	v_exp_f32_e32 v112, v112
	v_exp_f32_e32 v113, v113
	v_cvt_pk_bf16_f32 v76, v239, v242
	v_cvt_pk_bf16_f32 v77, v238, v240
	v_add_f32_e32 v229, v243, v245
	v_add_f32_e32 v229, v241, v229
	s_waitcnt lgkmcnt(6)
	v_mfma_f32_32x32x16_bf16 v[114:129], v[246:249], v[162:165], v[114:129]
	ds_read_b128 v[246:249], v220 offset:28672
	v_cvt_pk_bf16_f32 v66, v236, v237
	v_cvt_pk_bf16_f32 v67, v233, v235
	v_add_f32_e32 v229, v244, v229
	v_add_f32_e32 v229, v239, v229
	v_add_f32_e32 v229, v242, v229
	v_add_f32_e32 v229, v238, v229
	s_waitcnt lgkmcnt(6)
	v_mfma_f32_32x32x16_bf16 v[130:145], v[250:253], v[158:161], v[130:145]
	ds_read_b128 v[250:253], v220 offset:30720
	v_cvt_pk_bf16_f32 v68, v231, v234
	v_cvt_pk_bf16_f32 v69, v230, v232
	v_add_f32_e32 v229, v240, v229
	v_add_f32_e32 v229, v236, v229
	v_add_f32_e32 v229, v237, v229
	v_add_f32_e32 v229, v233, v229
	s_waitcnt lgkmcnt(6)
	v_mfma_f32_32x32x16_bf16 v[114:129], v[78:81], v[158:161], v[114:129]
	v_add_f32_e32 v229, v235, v229
	v_add_f32_e32 v229, v231, v229
	v_add_f32_e32 v229, v234, v229
	v_add_f32_e32 v229, v230, v229
	v_add_f32_e32 v229, v232, v229
	v_add_f32_e32 v229, v98, v229
	s_waitcnt lgkmcnt(5)
	v_mfma_f32_32x32x16_bf16 v[130:145], v[12:15], v[154:157], v[130:145]
	ds_read_b64_tr_b16 v[230:231], v213 offset:0
	ds_read_b64_tr_b16 v[232:233], v213 offset:1024
	ds_read_b64_tr_b16 v[234:235], v213 offset:2048
	ds_read_b64_tr_b16 v[236:237], v213 offset:3072
	v_add_f32_e32 v229, v99, v229
	v_add_f32_e32 v229, v100, v229
	v_add_f32_e32 v229, v101, v229
	s_waitcnt lgkmcnt(8)
	v_mfma_f32_32x32x16_bf16 v[114:129], v[4:7], v[154:157], v[114:129]
	ds_read_b64_tr_b16 v[238:239], v213 offset:4096
	ds_read_b64_tr_b16 v[240:241], v213 offset:5120
	ds_read_b64_tr_b16 v[242:243], v213 offset:6144
	ds_read_b64_tr_b16 v[244:245], v213 offset:7168
	v_add_f32_e32 v229, v102, v229
	v_add_f32_e32 v229, v103, v229
	v_add_f32_e32 v229, v104, v229
	s_waitcnt lgkmcnt(11)
	v_mfma_f32_32x32x16_bf16 v[130:145], v[8:11], v[150:153], v[130:145]
	v_add_f32_e32 v229, v105, v229
	v_add_f32_e32 v229, v106, v229
	v_add_f32_e32 v229, v107, v229
	v_add_f32_e32 v229, v108, v229
	v_add_f32_e32 v229, v109, v229
	v_add_f32_e32 v229, v110, v229
	s_waitcnt lgkmcnt(10)
	v_mfma_f32_32x32x16_bf16 v[114:129], v[174:177], v[150:153], v[114:129]
	v_add_f32_e32 v229, v111, v229
	v_add_f32_e32 v229, v112, v229
	v_add_f32_e32 v228, v113, v229
	s_add_i32 s36, s35, -1
	s_cmp_lt_u32 s36, s30
	s_cselect_b32 s0, 0, s30
	s_cselect_b32 s1, s29, s34
	s_lshl_b32 s0, s0, 6
	s_sub_i32 s37, s1, s0
	s_lshl_b32 s1, s36, 6
	s_add_i32 s37, s37, s1
	s_lshl_b32 s0, s37, 6
	s_add_u32 s48, s44, s0
	s_addc_u32 s49, s45, 0
	s_lshl_b32 s0, s37, 11
	s_add_u32 s46, s42, s0
	s_addc_u32 s47, s43, 0
	global_load_dwordx4 v[174:177], v226, s[48:49]
	s_waitcnt lgkmcnt(9)
	v_mfma_f32_32x32x16_bf16 v[130:145], v[246:249], v[146:149], v[130:145]
	v_cvt_pk_bf16_f32 v70, v98, v99
	v_cvt_pk_bf16_f32 v71, v100, v101
	v_cvt_pk_bf16_f32 v72, v102, v103
	v_cvt_pk_bf16_f32 v73, v104, v105
	global_load_dwordx4 v[8:11], v225, s[46:47]
	global_load_dwordx4 v[4:7], v225, s[46:47] offset:128
	s_waitcnt lgkmcnt(8)
	v_mfma_f32_32x32x16_bf16 v[114:129], v[250:253], v[146:149], v[114:129]
	v_cvt_pk_bf16_f32 v12, v106, v107
	v_cvt_pk_bf16_f32 v13, v108, v109
	v_cvt_pk_bf16_f32 v14, v110, v111
	v_cvt_pk_bf16_f32 v15, v112, v113
	ds_read_b64_tr_b16 v[78:79], v213 offset:512
	ds_read_b64_tr_b16 v[80:81], v213 offset:1536
	ds_read_b64_tr_b16 v[98:99], v213 offset:2560
	ds_read_b64_tr_b16 v[100:101], v213 offset:3584
	ds_read_b64_tr_b16 v[102:103], v213 offset:4608
	ds_read_b64_tr_b16 v[104:105], v213 offset:5632
	ds_read_b64_tr_b16 v[110:111], v213 offset:6656
	ds_read_b64_tr_b16 v[112:113], v213 offset:7680
	v_max3_f32 v2, v130, v131, v132
	v_max3_f32 v2, v2, v133, v134
	v_max3_f32 v2, v2, v135, v136
	v_max3_f32 v2, v2, v137, v138
	v_max3_f32 v2, v2, v139, v140
	v_max3_f32 v2, v2, v141, v142
	v_max3_f32 v2, v2, v143, v144
	v_max3_f32 v2, v2, v145, v114
	v_max3_f32 v2, v2, v115, v116
	s_waitcnt lgkmcnt(8)
	v_mfma_f32_32x32x16_bf16 v[50:65], v[230:233], v[74:77], v[50:65]
	v_max3_f32 v2, v2, v117, v118
	v_max3_f32 v2, v2, v119, v120
	v_max3_f32 v2, v2, v121, v122
	v_mfma_f32_32x32x16_bf16 v[50:65], v[234:237], v[66:69], v[50:65]
	v_max3_f32 v2, v2, v123, v124
	v_max3_f32 v2, v2, v125, v126
	v_max3_f32 v2, v2, v127, v128
	v_mfma_f32_32x32x16_bf16 v[50:65], v[238:241], v[70:73], v[50:65]
	v_max_f32_e32 v2, v2, v129
	v_mfma_f32_32x32x16_bf16 v[50:65], v[242:245], v[12:15], v[50:65]
	v_cmp_ge_f32_e32 vcc, s28, v2
	s_cmp_eq_u64 vcc, exec
	s_cbranch_scc0 .LBB0_542_0
	v_mov_b32_e32 v2, 1.0

; #define SBAR() __builtin_amdgcn_sched_barrier(0)
; #define ATT_PKN(P, BASE, OUT) do { u32x4 w = {cvt_pk_bf16(P[BASE + 0], P[BASE + 1]), cvt_pk_bf16(P[BASE + 2], P[BASE + 3]), cvt_pk_bf16(P[BASE + 4], P[BASE + 5]), cvt_pk_bf16(P[BASE + 6], P[BASE + 7])}; \
;     OUT = __builtin_bit_cast(bf16x8, w); } while (0)
; #define SLOAD(i, j) do { const int _row = KROW(j); skn[i] = *(const bf16x8*)(Knp + (size_t)(_row + sr) * ldk + c8 * 8); sv[i] = *(const bf16x8*)(Vp + (size_t)(_row + sr) * ldv + c8 * 8); \
;         if (krw) skr[i] = *(const bf16x8*)(Krp + (size_t)(_row + sr2) * 32 + c4 * 8); } while (0)
; #define SWRITEO(boff, i) do { *(LAS bf16x8*)(lds + (boff) + kn_st) = skn[i]; *(LAS bf16x8*)(lds + (boff) + v_stw) = sv[i]; if (krw) *(LAS bf16x8*)(lds + (boff) + kr_st) = skr[i]; } while (0)
; #define PVO(boff) do { pv_one<0>(o0, vb0 + (boff), pa0, pa1, pa2, pa3); pv_one<1>(o1, vb0 + (boff), pa0, pa1, pa2, pa3); } while (0)
; #define SWAIT() asm volatile("s_waitcnt vmcnt(2)" ::: "memory")
; __device__ __forceinline__ void finishSM(f32x16& p0, f32x16& p1, float alpha, float& l_reg, bf16x8& pa0, bf16x8& pa1, bf16x8& pa2, bf16x8& pa3) {
; #pragma unroll
;     for (int r = 0; r < 16; ++r) p1[r] = EXP_PROBE ? fmaf(p1[r], 0.001f, 1.f) : __builtin_amdgcn_exp2f(p1[r]);
;     float ps = 0.f;
; #pragma unroll
;     for (int r = 0; r < 16; ++r) ps += p0[r];
; #pragma unroll
;     for (int r = 0; r < 16; ++r) ps += p1[r];
;     { auto rr = __builtin_amdgcn_permlane32_swap(__float_as_uint(ps), __float_as_uint(ps), false, false);
;       ps = __uint_as_float(rr[0]) + __uint_as_float(rr[1]); }
;     l_reg = l_reg * alpha + ps;
;     ATT_PKN(p0, 0, pa0); ATT_PKN(p0, 8, pa1); ATT_PKN(p1, 0, pa2); ATT_PKN(p1, 8, pa3);
; }
; template <int DQK, bool FIXM> ...
;     ...
;         SBAR(); qkt<DQK>(pA0, pA1, lds + bK, qr, r32, hi, negm);
;         finishSM(pB0, pB1, alB, l_reg, pa0, pa1, pa2, pa3); SBAR();
;         if (j + 3 < NT) SLOAD(0, j + 3); SBAR();
;         if constexpr (FIXM) pv_psm<true>(o0, o1, vb0 + bV, pa0, pa1, pa2, pa3, pA0, pA1, m_reg, negm, alA); else { PVO(bV); partialSM<false>(pA0, pA1, m_reg, negm, alA); }
;         SWAIT(); SWRITEO(bW, 1);
.LBB0_531_0:
	s_waitcnt lgkmcnt(0)
	s_barrier
	ds_read_b128 v[178:181], v209 offset:40960
	ds_read_b128 v[182:185], v209 offset:45056
	ds_read_b128 v[170:173], v210 offset:40960
	ds_read_b128 v[66:69], v210 offset:45056
	ds_read_b128 v[70:73], v211 offset:40960
	ds_read_b128 v[74:77], v211 offset:45056
	ds_read_b128 v[78:81], v212 offset:40960
	v_exp_f32_e32 v114, v114
	v_exp_f32_e32 v115, v115
	v_exp_f32_e32 v116, v116
	v_exp_f32_e32 v117, v117
	v_exp_f32_e32 v118, v118
	v_exp_f32_e32 v119, v119
	v_exp_f32_e32 v120, v120
	v_exp_f32_e32 v121, v121
	s_waitcnt lgkmcnt(6)
	v_mfma_f32_32x32x16_bf16 v[130:145], v[178:181], v[166:169], v[82:97]
	ds_read_b128 v[178:181], v212 offset:45056
	v_exp_f32_e32 v122, v122
	v_exp_f32_e32 v123, v123
	v_exp_f32_e32 v124, v124
	v_cvt_pk_bf16_f32 v12, v16, v234
	s_waitcnt lgkmcnt(6)
	v_mfma_f32_32x32x16_bf16 v[98:113], v[182:185], v[166:169], v[82:97]
	ds_read_b128 v[182:185], v219 offset:49152
	v_exp_f32_e32 v125, v125
	v_exp_f32_e32 v126, v126
	v_exp_f32_e32 v127, v127
	v_cvt_pk_bf16_f32 v13, v235, v236
	s_waitcnt lgkmcnt(6)
	v_mfma_f32_32x32x16_bf16 v[130:145], v[170:173], v[162:165], v[130:145]
	ds_read_b128 v[170:173], v219 offset:51200
	v_exp_f32_e32 v128, v128
	v_exp_f32_e32 v129, v129
	v_cvt_pk_bf16_f32 v14, v237, v238
	v_cvt_pk_bf16_f32 v15, v239, v240
	v_add_f32_e32 v252, v16, v234
	v_add_f32_e32 v252, v235, v252
	s_waitcnt lgkmcnt(6)
	v_mfma_f32_32x32x16_bf16 v[98:113], v[66:69], v[162:165], v[98:113]
	ds_read_b128 v[66:69], v220 offset:49152
	v_cvt_pk_bf16_f32 v230, v241, v242
	v_cvt_pk_bf16_f32 v231, v243, v244
	v_add_f32_e32 v252, v236, v252
	v_add_f32_e32 v252, v237, v252
	v_add_f32_e32 v252, v238, v252
	v_add_f32_e32 v252, v239, v252
	s_waitcnt lgkmcnt(6)
	v_mfma_f32_32x32x16_bf16 v[130:145], v[70:73], v[158:161], v[130:145]
	ds_read_b128 v[70:73], v220 offset:51200
	v_cvt_pk_bf16_f32 v232, v245, v246
	v_cvt_pk_bf16_f32 v233, v247, v248
	v_add_f32_e32 v252, v240, v252
	v_add_f32_e32 v252, v241, v252
	v_add_f32_e32 v252, v242, v252
	v_add_f32_e32 v252, v243, v252
	s_waitcnt lgkmcnt(6)
	v_mfma_f32_32x32x16_bf16 v[98:113], v[74:77], v[158:161], v[98:113]
	v_add_f32_e32 v252, v244, v252
	v_add_f32_e32 v252, v245, v252
	v_add_f32_e32 v252, v246, v252
	v_add_f32_e32 v252, v247, v252
	v_add_f32_e32 v252, v248, v252
	v_add_f32_e32 v252, v114, v252
	s_waitcnt lgkmcnt(5)
	v_mfma_f32_32x32x16_bf16 v[130:145], v[78:81], v[154:157], v[130:145]
	ds_read_b64_tr_b16 v[234:235], v213 offset:20480
	ds_read_b64_tr_b16 v[236:237], v213 offset:21504
	ds_read_b64_tr_b16 v[238:239], v213 offset:22528
	ds_read_b64_tr_b16 v[240:241], v213 offset:23552
	v_add_f32_e32 v252, v115, v252
	v_add_f32_e32 v252, v116, v252
	v_add_f32_e32 v252, v117, v252
	s_waitcnt lgkmcnt(8)
	v_mfma_f32_32x32x16_bf16 v[98:113], v[178:181], v[154:157], v[98:113]
	ds_read_b64_tr_b16 v[242:243], v213 offset:24576
	ds_read_b64_tr_b16 v[244:245], v213 offset:25600
	ds_read_b64_tr_b16 v[246:247], v213 offset:26624
	ds_read_b64_tr_b16 v[248:249], v213 offset:27648
	v_add_f32_e32 v252, v118, v252
	v_add_f32_e32 v252, v119, v252
	v_add_f32_e32 v252, v120, v252
	s_waitcnt lgkmcnt(11)
	v_mfma_f32_32x32x16_bf16 v[130:145], v[182:185], v[150:153], v[130:145]
	v_add_f32_e32 v252, v121, v252
	v_add_f32_e32 v252, v122, v252
	v_add_f32_e32 v252, v123, v252
	v_add_f32_e32 v252, v124, v252
	v_add_f32_e32 v252, v125, v252
	v_add_f32_e32 v252, v126, v252
	s_waitcnt lgkmcnt(10)
	v_mfma_f32_32x32x16_bf16 v[98:113], v[170:173], v[150:153], v[98:113]
	v_add_f32_e32 v252, v127, v252
	v_add_f32_e32 v252, v128, v252
	s_waitcnt lgkmcnt(9)
	v_mfma_f32_32x32x16_bf16 v[130:145], v[66:69], v[146:149], v[130:145]
	v_cvt_pk_bf16_f32 v114, v114, v115
	v_cvt_pk_bf16_f32 v115, v116, v117
	v_cvt_pk_bf16_f32 v116, v118, v119
	v_cvt_pk_bf16_f32 v117, v120, v121
	s_cmp_ge_u32 s35, s31
	s_cbranch_scc1 .Lmla_b_noload_0
	s_cmp_lt_u32 s35, s30
	s_cselect_b32 s0, 0, s30
	s_cselect_b32 s1, s29, s34
	s_lshl_b32 s0, s0, 6
	s_sub_i32 s37, s1, s0
	s_lshl_b32 s1, s35, 6
	s_add_i32 s37, s37, s1
	s_lshl_b32 s0, s37, 6
	s_add_u32 s48, s44, s0
	s_addc_u32 s49, s45, 0
	s_lshl_b32 s0, s37, 11
	s_add_u32 s46, s42, s0
	s_addc_u32 s47, s43, 0
	global_load_dwordx4 v[170:173], v226, s[48:49]
	global_load_dwordx4 v[178:181], v225, s[46:47]
	global_load_dwordx4 v[182:185], v225, s[46:47] offset:128
.Lmla_b_ld_done_0:
	s_waitcnt lgkmcnt(8)
	v_mfma_f32_32x32x16_bf16 v[98:113], v[70:73], v[146:149], v[98:113]
	v_cvt_pk_bf16_f32 v118, v122, v123
	v_cvt_pk_bf16_f32 v119, v124, v125
	v_cvt_pk_bf16_f32 v120, v126, v127
	v_cvt_pk_bf16_f32 v121, v128, v129
	v_add_f32_e32 v126, v129, v252
	ds_read_b64_tr_b16 v[66:67], v213 offset:20992
	ds_read_b64_tr_b16 v[68:69], v213 offset:22016
	ds_read_b64_tr_b16 v[70:71], v213 offset:23040
	ds_read_b64_tr_b16 v[72:73], v213 offset:24064
	ds_read_b64_tr_b16 v[74:75], v213 offset:25088
	ds_read_b64_tr_b16 v[76:77], v213 offset:26112
	ds_read_b64_tr_b16 v[78:79], v213 offset:27136
	ds_read_b64_tr_b16 v[80:81], v213 offset:28160
	v_max3_f32 v250, v130, v131, v132
	v_max3_f32 v250, v250, v133, v134
	v_max3_f32 v250, v250, v135, v136
	v_max3_f32 v250, v250, v137, v138
	v_max3_f32 v250, v250, v139, v140
	v_max3_f32 v250, v250, v141, v142
	v_max3_f32 v250, v250, v143, v144
	v_max3_f32 v250, v250, v145, v98
	v_max3_f32 v250, v250, v99, v100
	s_waitcnt lgkmcnt(8)
	v_mfma_f32_32x32x16_bf16 v[50:65], v[234:237], v[12:15], v[50:65]
	v_max3_f32 v250, v250, v101, v102
	v_max3_f32 v250, v250, v103, v104
	v_max3_f32 v250, v250, v105, v106
	v_mfma_f32_32x32x16_bf16 v[50:65], v[238:241], v[230:233], v[50:65]
	v_max3_f32 v250, v250, v107, v108
	v_max3_f32 v250, v250, v109, v110
	v_max3_f32 v250, v250, v111, v112
	v_mfma_f32_32x32x16_bf16 v[50:65], v[242:245], v[114:117], v[50:65]
	v_max_f32_e32 v250, v250, v113
	v_mfma_f32_32x32x16_bf16 v[50:65], v[246:249], v[118:121], v[50:65]
	v_cmp_ge_f32_e32 vcc, s28, v250
	s_cmp_eq_u64 vcc, exec
	v_mov_b32_e32 v16, 1.0
	s_cbranch_scc0 .LBB0_543_0

; __device__ __forceinline__ void finishSM(f32x16& p0, f32x16& p1, float alpha, float& l_reg, bf16x8& pa0, bf16x8& pa1, bf16x8& pa2, bf16x8& pa3) {
; #pragma unroll
;     for (int r = 0; r < 16; ++r) p1[r] = EXP_PROBE ? fmaf(p1[r], 0.001f, 1.f) : __builtin_amdgcn_exp2f(p1[r]);
;     float ps = 0.f;
; #pragma unroll
;     for (int r = 0; r < 16; ++r) ps += p0[r];
; #pragma unroll
;     for (int r = 0; r < 16; ++r) ps += p1[r];
;     { auto rr = __builtin_amdgcn_permlane32_swap(__float_as_uint(ps), __float_as_uint(ps), false, false);
;       ps = __uint_as_float(rr[0]) + __uint_as_float(rr[1]); }
;     l_reg = l_reg * alpha + ps;
;     ATT_PKN(p0, 0, pa0); ATT_PKN(p0, 8, pa1); ATT_PKN(p1, 0, pa2); ATT_PKN(p1, 8, pa3);
; }
; template <int DQK> __device__ __forceinline__ void qkt(f32x16& p0, f32x16& p1, const LAS char* buf, const bf16x8* qr, int r32, int hi, const f32x16& negm) {
; #pragma unroll
;     for (int d0 = 0; d0 < 4; ++d0) { const int ch = d0 * 2 + hi;
;         const bf16x8 b0 = *(const LAS bf16x8*)(buf + B_KN + swz64(r32, ch));
;         const bf16x8 b1 = *(const LAS bf16x8*)(buf + B_KN + swz64(32 + r32, ch));
;         p0 = __builtin_amdgcn_mfma_f32_32x32x16_bf16(b0, qr[d0], d0 == 0 ? negm : p0, 0, 0, 0);
;         p1 = __builtin_amdgcn_mfma_f32_32x32x16_bf16(b1, qr[d0], d0 == 0 ? negm : p1, 0, 0, 0); }
;     if constexpr (DQK == 96) {
; #pragma unroll
;         for (int d0 = 0; d0 < 2; ++d0) { const int ch = d0 * 2 + hi;
;             const bf16x8 b0 = *(const LAS bf16x8*)(buf + B_KR + swz32(r32, ch));
;             const bf16x8 b1 = *(const LAS bf16x8*)(buf + B_KR + swz32(32 + r32, ch));
;             p0 = __builtin_amdgcn_mfma_f32_32x32x16_bf16(b0, qr[4 + d0], p0, 0, 0, 0);
;             p1 = __builtin_amdgcn_mfma_f32_32x32x16_bf16(b1, qr[4 + d0], p1, 0, 0, 0); }
;     }
; }
; template <int D0> __device__ __forceinline__ void pv_one(f32x16& od, unsigned vb, bf16x8 pa0, bf16x8 pa1, bf16x8 pa2, bf16x8 pa3) {
;     const s16x4 l0 = tr_read<v_rd_off(D0, 0, 0)>(vb), h0 = tr_read<v_rd_off(D0, 0, 1)>(vb), l1 = tr_read<v_rd_off(D0, 1, 0)>(vb), h1 = tr_read<v_rd_off(D0, 1, 1)>(vb);
;     const s16x4 l2 = tr_read<v_rd_off(D0, 2, 0)>(vb), h2 = tr_read<v_rd_off(D0, 2, 1)>(vb), l3 = tr_read<v_rd_off(D0, 3, 0)>(vb), h3 = tr_read<v_rd_off(D0, 3, 1)>(vb);
;     asm volatile("s_waitcnt lgkmcnt(0)" ::: "memory"); SBAR();
.LBB0_540_0:
	v_fmac_f32_e32 v228, v227, v223
	s_add_i32 s35, s35, 2
	v_fma_f32 v223, v228, v2, v126
	s_cmp_ge_u32 s36, s12
	s_cbranch_scc1 .Lmla_exit_0
	v_mov_b32_e32 v227, v16
	s_waitcnt lgkmcnt(0)
	s_barrier
	ds_read_b128 v[4:7], v209 offset:0
	ds_read_b128 v[8:11], v209 offset:4096
	ds_read_b128 v[174:177], v210 offset:0
	ds_read_b128 v[246:249], v210 offset:4096
	ds_read_b128 v[250:253], v211 offset:0
	ds_read_b128 v[78:81], v211 offset:4096
	ds_read_b128 v[12:15], v212 offset:0
	v_exp_f32_e32 v98, v98
	v_exp_f32_e32 v99, v99
	v_exp_f32_e32 v100, v100
	v_exp_f32_e32 v101, v101
	v_exp_f32_e32 v102, v102
	v_exp_f32_e32 v103, v103
	v_exp_f32_e32 v104, v104
	v_exp_f32_e32 v105, v105
	s_waitcnt lgkmcnt(6)
	v_mfma_f32_32x32x16_bf16 v[130:145], v[4:7], v[166:169], v[82:97]
	ds_read_b128 v[4:7], v212 offset:4096
	v_exp_f32_e32 v106, v106
	v_exp_f32_e32 v107, v107
	v_exp_f32_e32 v108, v108
	v_cvt_pk_bf16_f32 v74, v243, v245
	s_waitcnt lgkmcnt(6)
	v_mfma_f32_32x32x16_bf16 v[114:129], v[8:11], v[166:169], v[82:97]
	ds_read_b128 v[8:11], v219 offset:8192
	v_exp_f32_e32 v109, v109
	v_exp_f32_e32 v110, v110
	v_exp_f32_e32 v111, v111
	v_cvt_pk_bf16_f32 v75, v241, v244
	s_waitcnt lgkmcnt(6)
	v_mfma_f32_32x32x16_bf16 v[130:145], v[174:177], v[162:165], v[130:145]
	ds_read_b128 v[174:177], v219 offset:10240
	v_exp_f32_e32 v112, v112
	v_exp_f32_e32 v113, v113
	v_cvt_pk_bf16_f32 v76, v239, v242
	v_cvt_pk_bf16_f32 v77, v238, v240
	v_add_f32_e32 v229, v243, v245
	v_add_f32_e32 v229, v241, v229
	s_waitcnt lgkmcnt(6)
	v_mfma_f32_32x32x16_bf16 v[114:129], v[246:249], v[162:165], v[114:129]
	ds_read_b128 v[246:249], v220 offset:8192
	v_cvt_pk_bf16_f32 v66, v236, v237
	v_cvt_pk_bf16_f32 v67, v233, v235
	v_add_f32_e32 v229, v244, v229
	v_add_f32_e32 v229, v239, v229
	v_add_f32_e32 v229, v242, v229
	v_add_f32_e32 v229, v238, v229
	s_waitcnt lgkmcnt(6)
	v_mfma_f32_32x32x16_bf16 v[130:145], v[250:253], v[158:161], v[130:145]
	ds_read_b128 v[250:253], v220 offset:10240
	v_cvt_pk_bf16_f32 v68, v231, v234
	v_cvt_pk_bf16_f32 v69, v230, v232
	v_add_f32_e32 v229, v240, v229
	v_add_f32_e32 v229, v236, v229
	v_add_f32_e32 v229, v237, v229
	v_add_f32_e32 v229, v233, v229
	s_waitcnt lgkmcnt(6)
	v_mfma_f32_32x32x16_bf16 v[114:129], v[78:81], v[158:161], v[114:129]
	v_add_f32_e32 v229, v235, v229
	v_add_f32_e32 v229, v231, v229
	v_add_f32_e32 v229, v234, v229
	v_add_f32_e32 v229, v230, v229
	v_add_f32_e32 v229, v232, v229
	v_add_f32_e32 v229, v98, v229
	s_waitcnt lgkmcnt(5)
	v_mfma_f32_32x32x16_bf16 v[130:145], v[12:15], v[154:157], v[130:145]
	ds_read_b64_tr_b16 v[230:231], v213 offset:40960
	ds_read_b64_tr_b16 v[232:233], v213 offset:41984
	ds_read_b64_tr_b16 v[234:235], v213 offset:43008
	ds_read_b64_tr_b16 v[236:237], v213 offset:44032
	v_add_f32_e32 v229, v99, v229
	v_add_f32_e32 v229, v100, v229
	v_add_f32_e32 v229, v101, v229
	s_waitcnt lgkmcnt(8)
	v_mfma_f32_32x32x16_bf16 v[114:129], v[4:7], v[154:157], v[114:129]
	ds_read_b64_tr_b16 v[238:239], v213 offset:45056
	ds_read_b64_tr_b16 v[240:241], v213 offset:46080
	ds_read_b64_tr_b16 v[242:243], v213 offset:47104
	ds_read_b64_tr_b16 v[244:245], v213 offset:48128
	v_add_f32_e32 v229, v102, v229
	v_add_f32_e32 v229, v103, v229
	v_add_f32_e32 v229, v104, v229
	s_waitcnt lgkmcnt(11)
	v_mfma_f32_32x32x16_bf16 v[130:145], v[8:11], v[150:153], v[130:145]
	v_add_f32_e32 v229, v105, v229
	v_add_f32_e32 v229, v106, v229
	v_add_f32_e32 v229, v107, v229
	v_add_f32_e32 v229, v108, v229
	v_add_f32_e32 v229, v109, v229
	v_add_f32_e32 v229, v110, v229
	s_waitcnt lgkmcnt(10)
	v_mfma_f32_32x32x16_bf16 v[114:129], v[174:177], v[150:153], v[114:129]
	v_add_f32_e32 v229, v111, v229
	v_add_f32_e32 v229, v112, v229
	v_add_f32_e32 v228, v113, v229
	s_add_i32 s36, s35, -1
	s_cmp_lt_u32 s36, s30
	s_cselect_b32 s0, 0, s30
	s_cselect_b32 s1, s29, s34
	s_lshl_b32 s0, s0, 6
	s_sub_i32 s37, s1, s0
	s_lshl_b32 s1, s36, 6
	s_add_i32 s37, s37, s1
	s_lshl_b32 s0, s37, 6
	s_add_u32 s48, s44, s0
	s_addc_u32 s49, s45, 0
	s_lshl_b32 s0, s37, 11
	s_add_u32 s46, s42, s0
	s_addc_u32 s47, s43, 0
	global_load_dwordx4 v[174:177], v226, s[48:49]
	s_waitcnt lgkmcnt(9)
	v_mfma_f32_32x32x16_bf16 v[130:145], v[246:249], v[146:149], v[130:145]
	v_cvt_pk_bf16_f32 v70, v98, v99
	v_cvt_pk_bf16_f32 v71, v100, v101
	v_cvt_pk_bf16_f32 v72, v102, v103
	v_cvt_pk_bf16_f32 v73, v104, v105
	global_load_dwordx4 v[8:11], v225, s[46:47]
	global_load_dwordx4 v[4:7], v225, s[46:47] offset:128
	s_waitcnt lgkmcnt(8)
	v_mfma_f32_32x32x16_bf16 v[114:129], v[250:253], v[146:149], v[114:129]
	v_cvt_pk_bf16_f32 v12, v106, v107
	v_cvt_pk_bf16_f32 v13, v108, v109
	v_cvt_pk_bf16_f32 v14, v110, v111
	v_cvt_pk_bf16_f32 v15, v112, v113
	ds_read_b64_tr_b16 v[78:79], v213 offset:41472
	ds_read_b64_tr_b16 v[80:81], v213 offset:42496
	ds_read_b64_tr_b16 v[98:99], v213 offset:43520
	ds_read_b64_tr_b16 v[100:101], v213 offset:44544
	ds_read_b64_tr_b16 v[102:103], v213 offset:45568
	ds_read_b64_tr_b16 v[104:105], v213 offset:46592
	ds_read_b64_tr_b16 v[110:111], v213 offset:47616
	ds_read_b64_tr_b16 v[112:113], v213 offset:48640
	v_max3_f32 v2, v130, v131, v132
	v_max3_f32 v2, v2, v133, v134
	v_max3_f32 v2, v2, v135, v136
	v_max3_f32 v2, v2, v137, v138
	v_max3_f32 v2, v2, v139, v140
	v_max3_f32 v2, v2, v141, v142
	v_max3_f32 v2, v2, v143, v144
	v_max3_f32 v2, v2, v145, v114
	v_max3_f32 v2, v2, v115, v116
	s_waitcnt lgkmcnt(8)
	v_mfma_f32_32x32x16_bf16 v[50:65], v[230:233], v[74:77], v[50:65]
	v_max3_f32 v2, v2, v117, v118
	v_max3_f32 v2, v2, v119, v120
	v_max3_f32 v2, v2, v121, v122
	v_mfma_f32_32x32x16_bf16 v[50:65], v[234:237], v[66:69], v[50:65]
	v_max3_f32 v2, v2, v123, v124
	v_max3_f32 v2, v2, v125, v126
	v_max3_f32 v2, v2, v127, v128
	v_mfma_f32_32x32x16_bf16 v[50:65], v[238:241], v[70:73], v[50:65]
	v_max_f32_e32 v2, v2, v129
	v_mfma_f32_32x32x16_bf16 v[50:65], v[242:245], v[12:15], v[50:65]
	v_cmp_ge_f32_e32 vcc, s28, v2
	s_cmp_eq_u64 vcc, exec
	s_cbranch_scc0 .LBB0_542_1
	v_mov_b32_e32 v2, 1.0

; __device__ __forceinline__ void finishSM(f32x16& p0, f32x16& p1, float alpha, float& l_reg, bf16x8& pa0, bf16x8& pa1, bf16x8& pa2, bf16x8& pa3) {
; #pragma unroll
;     for (int r = 0; r < 16; ++r) p1[r] = EXP_PROBE ? fmaf(p1[r], 0.001f, 1.f) : __builtin_amdgcn_exp2f(p1[r]);
;     float ps = 0.f;
; #pragma unroll
;     for (int r = 0; r < 16; ++r) ps += p0[r];
; #pragma unroll
;     for (int r = 0; r < 16; ++r) ps += p1[r];
;     { auto rr = __builtin_amdgcn_permlane32_swap(__float_as_uint(ps), __float_as_uint(ps), false, false);
;       ps = __uint_as_float(rr[0]) + __uint_as_float(rr[1]); }
;     l_reg = l_reg * alpha + ps;
;     ATT_PKN(p0, 0, pa0); ATT_PKN(p0, 8, pa1); ATT_PKN(p1, 0, pa2); ATT_PKN(p1, 8, pa3);
; }
; template <int DQK> __device__ __forceinline__ void qkt(f32x16& p0, f32x16& p1, const LAS char* buf, const bf16x8* qr, int r32, int hi, const f32x16& negm) {
; #pragma unroll
;     for (int d0 = 0; d0 < 4; ++d0) { const int ch = d0 * 2 + hi;
;         const bf16x8 b0 = *(const LAS bf16x8*)(buf + B_KN + swz64(r32, ch));
;         const bf16x8 b1 = *(const LAS bf16x8*)(buf + B_KN + swz64(32 + r32, ch));
;         p0 = __builtin_amdgcn_mfma_f32_32x32x16_bf16(b0, qr[d0], d0 == 0 ? negm : p0, 0, 0, 0);
;         p1 = __builtin_amdgcn_mfma_f32_32x32x16_bf16(b1, qr[d0], d0 == 0 ? negm : p1, 0, 0, 0); }
;     if constexpr (DQK == 96) {
; #pragma unroll
;         for (int d0 = 0; d0 < 2; ++d0) { const int ch = d0 * 2 + hi;
;             const bf16x8 b0 = *(const LAS bf16x8*)(buf + B_KR + swz32(r32, ch));
;             const bf16x8 b1 = *(const LAS bf16x8*)(buf + B_KR + swz32(32 + r32, ch));
;             p0 = __builtin_amdgcn_mfma_f32_32x32x16_bf16(b0, qr[4 + d0], p0, 0, 0, 0);
;             p1 = __builtin_amdgcn_mfma_f32_32x32x16_bf16(b1, qr[4 + d0], p1, 0, 0, 0); }
;     }
; }
; template <int D0> __device__ __forceinline__ void pv_one(f32x16& od, unsigned vb, bf16x8 pa0, bf16x8 pa1, bf16x8 pa2, bf16x8 pa3) {
;     const s16x4 l0 = tr_read<v_rd_off(D0, 0, 0)>(vb), h0 = tr_read<v_rd_off(D0, 0, 1)>(vb), l1 = tr_read<v_rd_off(D0, 1, 0)>(vb), h1 = tr_read<v_rd_off(D0, 1, 1)>(vb);
;     const s16x4 l2 = tr_read<v_rd_off(D0, 2, 0)>(vb), h2 = tr_read<v_rd_off(D0, 2, 1)>(vb), l3 = tr_read<v_rd_off(D0, 3, 0)>(vb), h3 = tr_read<v_rd_off(D0, 3, 1)>(vb);
;     asm volatile("s_waitcnt lgkmcnt(0)" ::: "memory"); SBAR();
.LBB0_531_1:
	s_waitcnt lgkmcnt(0)
	s_barrier
	ds_read_b128 v[178:181], v209 offset:20480
	ds_read_b128 v[182:185], v209 offset:24576
	ds_read_b128 v[170:173], v210 offset:20480
	ds_read_b128 v[66:69], v210 offset:24576
	ds_read_b128 v[70:73], v211 offset:20480
	ds_read_b128 v[74:77], v211 offset:24576
	ds_read_b128 v[78:81], v212 offset:20480
	v_exp_f32_e32 v114, v114
	v_exp_f32_e32 v115, v115
	v_exp_f32_e32 v116, v116
	v_exp_f32_e32 v117, v117
	v_exp_f32_e32 v118, v118
	v_exp_f32_e32 v119, v119
	v_exp_f32_e32 v120, v120
	v_exp_f32_e32 v121, v121
	s_waitcnt lgkmcnt(6)
	v_mfma_f32_32x32x16_bf16 v[130:145], v[178:181], v[166:169], v[82:97]
	ds_read_b128 v[178:181], v212 offset:24576
	v_exp_f32_e32 v122, v122
	v_exp_f32_e32 v123, v123
	v_exp_f32_e32 v124, v124
	v_cvt_pk_bf16_f32 v12, v16, v234
	s_waitcnt lgkmcnt(6)
	v_mfma_f32_32x32x16_bf16 v[98:113], v[182:185], v[166:169], v[82:97]
	ds_read_b128 v[182:185], v219 offset:28672
	v_exp_f32_e32 v125, v125
	v_exp_f32_e32 v126, v126
	v_exp_f32_e32 v127, v127
	v_cvt_pk_bf16_f32 v13, v235, v236
	s_waitcnt lgkmcnt(6)
	v_mfma_f32_32x32x16_bf16 v[130:145], v[170:173], v[162:165], v[130:145]
	ds_read_b128 v[170:173], v219 offset:30720
	v_exp_f32_e32 v128, v128
	v_exp_f32_e32 v129, v129
	v_cvt_pk_bf16_f32 v14, v237, v238
	v_cvt_pk_bf16_f32 v15, v239, v240
	v_add_f32_e32 v252, v16, v234
	v_add_f32_e32 v252, v235, v252
	s_waitcnt lgkmcnt(6)
	v_mfma_f32_32x32x16_bf16 v[98:113], v[66:69], v[162:165], v[98:113]
	ds_read_b128 v[66:69], v220 offset:28672
	v_cvt_pk_bf16_f32 v230, v241, v242
	v_cvt_pk_bf16_f32 v231, v243, v244
	v_add_f32_e32 v252, v236, v252
	v_add_f32_e32 v252, v237, v252
	v_add_f32_e32 v252, v238, v252
	v_add_f32_e32 v252, v239, v252
	s_waitcnt lgkmcnt(6)
	v_mfma_f32_32x32x16_bf16 v[130:145], v[70:73], v[158:161], v[130:145]
	ds_read_b128 v[70:73], v220 offset:30720
	v_cvt_pk_bf16_f32 v232, v245, v246
	v_cvt_pk_bf16_f32 v233, v247, v248
	v_add_f32_e32 v252, v240, v252
	v_add_f32_e32 v252, v241, v252
	v_add_f32_e32 v252, v242, v252
	v_add_f32_e32 v252, v243, v252
	s_waitcnt lgkmcnt(6)
	v_mfma_f32_32x32x16_bf16 v[98:113], v[74:77], v[158:161], v[98:113]
	v_add_f32_e32 v252, v244, v252
	v_add_f32_e32 v252, v245, v252
	v_add_f32_e32 v252, v246, v252
	v_add_f32_e32 v252, v247, v252
	v_add_f32_e32 v252, v248, v252
	v_add_f32_e32 v252, v114, v252
	s_waitcnt lgkmcnt(5)
	v_mfma_f32_32x32x16_bf16 v[130:145], v[78:81], v[154:157], v[130:145]
	ds_read_b64_tr_b16 v[234:235], v213 offset:0
	ds_read_b64_tr_b16 v[236:237], v213 offset:1024
	ds_read_b64_tr_b16 v[238:239], v213 offset:2048
	ds_read_b64_tr_b16 v[240:241], v213 offset:3072
	v_add_f32_e32 v252, v115, v252
	v_add_f32_e32 v252, v116, v252
	v_add_f32_e32 v252, v117, v252
	s_waitcnt lgkmcnt(8)
	v_mfma_f32_32x32x16_bf16 v[98:113], v[178:181], v[154:157], v[98:113]
	ds_read_b64_tr_b16 v[242:243], v213 offset:4096
	ds_read_b64_tr_b16 v[244:245], v213 offset:5120
	ds_read_b64_tr_b16 v[246:247], v213 offset:6144
	ds_read_b64_tr_b16 v[248:249], v213 offset:7168
	v_add_f32_e32 v252, v118, v252
	v_add_f32_e32 v252, v119, v252
	v_add_f32_e32 v252, v120, v252
	s_waitcnt lgkmcnt(11)
	v_mfma_f32_32x32x16_bf16 v[130:145], v[182:185], v[150:153], v[130:145]
	v_add_f32_e32 v252, v121, v252
	v_add_f32_e32 v252, v122, v252
	v_add_f32_e32 v252, v123, v252
	v_add_f32_e32 v252, v124, v252
	v_add_f32_e32 v252, v125, v252
	v_add_f32_e32 v252, v126, v252
	s_waitcnt lgkmcnt(10)
	v_mfma_f32_32x32x16_bf16 v[98:113], v[170:173], v[150:153], v[98:113]
	v_add_f32_e32 v252, v127, v252
	v_add_f32_e32 v252, v128, v252
	s_waitcnt lgkmcnt(9)
	v_mfma_f32_32x32x16_bf16 v[130:145], v[66:69], v[146:149], v[130:145]
	v_cvt_pk_bf16_f32 v114, v114, v115
	v_cvt_pk_bf16_f32 v115, v116, v117
	v_cvt_pk_bf16_f32 v116, v118, v119
	v_cvt_pk_bf16_f32 v117, v120, v121
	s_cmp_ge_u32 s35, s31
	s_cbranch_scc1 .Lmla_b_noload_1
	s_cmp_lt_u32 s35, s30
	s_cselect_b32 s0, 0, s30
	s_cselect_b32 s1, s29, s34
	s_lshl_b32 s0, s0, 6
	s_sub_i32 s37, s1, s0
	s_lshl_b32 s1, s35, 6
	s_add_i32 s37, s37, s1
	s_lshl_b32 s0, s37, 6
	s_add_u32 s48, s44, s0
	s_addc_u32 s49, s45, 0
	s_lshl_b32 s0, s37, 11
	s_add_u32 s46, s42, s0
	s_addc_u32 s47, s43, 0
	global_load_dwordx4 v[170:173], v226, s[48:49]
	global_load_dwordx4 v[178:181], v225, s[46:47]
	global_load_dwordx4 v[182:185], v225, s[46:47] offset:128
.Lmla_b_ld_done_1:
	s_waitcnt lgkmcnt(8)
	v_mfma_f32_32x32x16_bf16 v[98:113], v[70:73], v[146:149], v[98:113]
	v_cvt_pk_bf16_f32 v118, v122, v123
	v_cvt_pk_bf16_f32 v119, v124, v125
	v_cvt_pk_bf16_f32 v120, v126, v127
	v_cvt_pk_bf16_f32 v121, v128, v129
	v_add_f32_e32 v126, v129, v252
	ds_read_b64_tr_b16 v[66:67], v213 offset:512
	ds_read_b64_tr_b16 v[68:69], v213 offset:1536
	ds_read_b64_tr_b16 v[70:71], v213 offset:2560
	ds_read_b64_tr_b16 v[72:73], v213 offset:3584
	ds_read_b64_tr_b16 v[74:75], v213 offset:4608
	ds_read_b64_tr_b16 v[76:77], v213 offset:5632
	ds_read_b64_tr_b16 v[78:79], v213 offset:6656
	ds_read_b64_tr_b16 v[80:81], v213 offset:7680
	v_max3_f32 v250, v130, v131, v132
	v_max3_f32 v250, v250, v133, v134
	v_max3_f32 v250, v250, v135, v136
	v_max3_f32 v250, v250, v137, v138
	v_max3_f32 v250, v250, v139, v140
	v_max3_f32 v250, v250, v141, v142
	v_max3_f32 v250, v250, v143, v144
	v_max3_f32 v250, v250, v145, v98
	v_max3_f32 v250, v250, v99, v100
	s_waitcnt lgkmcnt(8)
	v_mfma_f32_32x32x16_bf16 v[50:65], v[234:237], v[12:15], v[50:65]
	v_max3_f32 v250, v250, v101, v102
	v_max3_f32 v250, v250, v103, v104
	v_max3_f32 v250, v250, v105, v106
	v_mfma_f32_32x32x16_bf16 v[50:65], v[238:241], v[230:233], v[50:65]
	v_max3_f32 v250, v250, v107, v108
	v_max3_f32 v250, v250, v109, v110
	v_max3_f32 v250, v250, v111, v112
	v_mfma_f32_32x32x16_bf16 v[50:65], v[242:245], v[114:117], v[50:65]
	v_max_f32_e32 v250, v250, v113
	v_mfma_f32_32x32x16_bf16 v[50:65], v[246:249], v[118:121], v[50:65]
	v_cmp_ge_f32_e32 vcc, s28, v250
	s_cmp_eq_u64 vcc, exec
	v_mov_b32_e32 v16, 1.0
	s_cbranch_scc0 .LBB0_543_1

; __device__ __forceinline__ void finishSM(f32x16& p0, f32x16& p1, float alpha, float& l_reg, bf16x8& pa0, bf16x8& pa1, bf16x8& pa2, bf16x8& pa3) {
; #pragma unroll
;     for (int r = 0; r < 16; ++r) p1[r] = EXP_PROBE ? fmaf(p1[r], 0.001f, 1.f) : __builtin_amdgcn_exp2f(p1[r]);
;     float ps = 0.f;
; #pragma unroll
;     for (int r = 0; r < 16; ++r) ps += p0[r];
; #pragma unroll
;     for (int r = 0; r < 16; ++r) ps += p1[r];
;     { auto rr = __builtin_amdgcn_permlane32_swap(__float_as_uint(ps), __float_as_uint(ps), false, false);
;       ps = __uint_as_float(rr[0]) + __uint_as_float(rr[1]); }
;     l_reg = l_reg * alpha + ps;
;     ATT_PKN(p0, 0, pa0); ATT_PKN(p0, 8, pa1); ATT_PKN(p1, 0, pa2); ATT_PKN(p1, 8, pa3);
; }
; template <int DQK> __device__ __forceinline__ void qkt(f32x16& p0, f32x16& p1, const LAS char* buf, const bf16x8* qr, int r32, int hi, const f32x16& negm) {
; #pragma unroll
;     for (int d0 = 0; d0 < 4; ++d0) { const int ch = d0 * 2 + hi;
;         const bf16x8 b0 = *(const LAS bf16x8*)(buf + B_KN + swz64(r32, ch));
;         const bf16x8 b1 = *(const LAS bf16x8*)(buf + B_KN + swz64(32 + r32, ch));
;         p0 = __builtin_amdgcn_mfma_f32_32x32x16_bf16(b0, qr[d0], d0 == 0 ? negm : p0, 0, 0, 0);
;         p1 = __builtin_amdgcn_mfma_f32_32x32x16_bf16(b1, qr[d0], d0 == 0 ? negm : p1, 0, 0, 0); }
;     if constexpr (DQK == 96) {
; #pragma unroll
;         for (int d0 = 0; d0 < 2; ++d0) { const int ch = d0 * 2 + hi;
;             const bf16x8 b0 = *(const LAS bf16x8*)(buf + B_KR + swz32(r32, ch));
;             const bf16x8 b1 = *(const LAS bf16x8*)(buf + B_KR + swz32(32 + r32, ch));
;             p0 = __builtin_amdgcn_mfma_f32_32x32x16_bf16(b0, qr[4 + d0], p0, 0, 0, 0);
;             p1 = __builtin_amdgcn_mfma_f32_32x32x16_bf16(b1, qr[4 + d0], p1, 0, 0, 0); }
;     }
; }
; template <int D0> __device__ __forceinline__ void pv_one(f32x16& od, unsigned vb, bf16x8 pa0, bf16x8 pa1, bf16x8 pa2, bf16x8 pa3) {
;     const s16x4 l0 = tr_read<v_rd_off(D0, 0, 0)>(vb), h0 = tr_read<v_rd_off(D0, 0, 1)>(vb), l1 = tr_read<v_rd_off(D0, 1, 0)>(vb), h1 = tr_read<v_rd_off(D0, 1, 1)>(vb);
;     const s16x4 l2 = tr_read<v_rd_off(D0, 2, 0)>(vb), h2 = tr_read<v_rd_off(D0, 2, 1)>(vb), l3 = tr_read<v_rd_off(D0, 3, 0)>(vb), h3 = tr_read<v_rd_off(D0, 3, 1)>(vb);
;     asm volatile("s_waitcnt lgkmcnt(0)" ::: "memory"); SBAR();
.LBB0_540_1:
	v_fmac_f32_e32 v228, v227, v223
	s_add_i32 s35, s35, 2
	v_fma_f32 v223, v228, v2, v126
	s_cmp_ge_u32 s36, s12
	s_cbranch_scc1 .Lmla_exit_1
	v_mov_b32_e32 v227, v16
	s_waitcnt lgkmcnt(0)
	s_barrier
	ds_read_b128 v[4:7], v209 offset:40960
	ds_read_b128 v[8:11], v209 offset:45056
	ds_read_b128 v[174:177], v210 offset:40960
	ds_read_b128 v[246:249], v210 offset:45056
	ds_read_b128 v[250:253], v211 offset:40960
	ds_read_b128 v[78:81], v211 offset:45056
	ds_read_b128 v[12:15], v212 offset:40960
	v_exp_f32_e32 v98, v98
	v_exp_f32_e32 v99, v99
	v_exp_f32_e32 v100, v100
	v_exp_f32_e32 v101, v101
	v_exp_f32_e32 v102, v102
	v_exp_f32_e32 v103, v103
	v_exp_f32_e32 v104, v104
	v_exp_f32_e32 v105, v105
	s_waitcnt lgkmcnt(6)
	v_mfma_f32_32x32x16_bf16 v[130:145], v[4:7], v[166:169], v[82:97]
	ds_read_b128 v[4:7], v212 offset:45056
	v_exp_f32_e32 v106, v106
	v_exp_f32_e32 v107, v107
	v_exp_f32_e32 v108, v108
	v_cvt_pk_bf16_f32 v74, v243, v245
	s_waitcnt lgkmcnt(6)
	v_mfma_f32_32x32x16_bf16 v[114:129], v[8:11], v[166:169], v[82:97]
	ds_read_b128 v[8:11], v219 offset:49152
	v_exp_f32_e32 v109, v109
	v_exp_f32_e32 v110, v110
	v_exp_f32_e32 v111, v111
	v_cvt_pk_bf16_f32 v75, v241, v244
	s_waitcnt lgkmcnt(6)
	v_mfma_f32_32x32x16_bf16 v[130:145], v[174:177], v[162:165], v[130:145]
	ds_read_b128 v[174:177], v219 offset:51200
	v_exp_f32_e32 v112, v112
	v_exp_f32_e32 v113, v113
	v_cvt_pk_bf16_f32 v76, v239, v242
	v_cvt_pk_bf16_f32 v77, v238, v240
	v_add_f32_e32 v229, v243, v245
	v_add_f32_e32 v229, v241, v229
	s_waitcnt lgkmcnt(6)
	v_mfma_f32_32x32x16_bf16 v[114:129], v[246:249], v[162:165], v[114:129]
	ds_read_b128 v[246:249], v220 offset:49152
	v_cvt_pk_bf16_f32 v66, v236, v237
	v_cvt_pk_bf16_f32 v67, v233, v235
	v_add_f32_e32 v229, v244, v229
	v_add_f32_e32 v229, v239, v229
	v_add_f32_e32 v229, v242, v229
	v_add_f32_e32 v229, v238, v229
	s_waitcnt lgkmcnt(6)
	v_mfma_f32_32x32x16_bf16 v[130:145], v[250:253], v[158:161], v[130:145]
	ds_read_b128 v[250:253], v220 offset:51200
	v_cvt_pk_bf16_f32 v68, v231, v234
	v_cvt_pk_bf16_f32 v69, v230, v232
	v_add_f32_e32 v229, v240, v229
	v_add_f32_e32 v229, v236, v229
	v_add_f32_e32 v229, v237, v229
	v_add_f32_e32 v229, v233, v229
	s_waitcnt lgkmcnt(6)
	v_mfma_f32_32x32x16_bf16 v[114:129], v[78:81], v[158:161], v[114:129]
	v_add_f32_e32 v229, v235, v229
	v_add_f32_e32 v229, v231, v229
	v_add_f32_e32 v229, v234, v229
	v_add_f32_e32 v229, v230, v229
	v_add_f32_e32 v229, v232, v229
	v_add_f32_e32 v229, v98, v229
	s_waitcnt lgkmcnt(5)
	v_mfma_f32_32x32x16_bf16 v[130:145], v[12:15], v[154:157], v[130:145]
	ds_read_b64_tr_b16 v[230:231], v213 offset:20480
	ds_read_b64_tr_b16 v[232:233], v213 offset:21504
	ds_read_b64_tr_b16 v[234:235], v213 offset:22528
	ds_read_b64_tr_b16 v[236:237], v213 offset:23552
	v_add_f32_e32 v229, v99, v229
	v_add_f32_e32 v229, v100, v229
	v_add_f32_e32 v229, v101, v229
	s_waitcnt lgkmcnt(8)
	v_mfma_f32_32x32x16_bf16 v[114:129], v[4:7], v[154:157], v[114:129]
	ds_read_b64_tr_b16 v[238:239], v213 offset:24576
	ds_read_b64_tr_b16 v[240:241], v213 offset:25600
	ds_read_b64_tr_b16 v[242:243], v213 offset:26624
	ds_read_b64_tr_b16 v[244:245], v213 offset:27648
	v_add_f32_e32 v229, v102, v229
	v_add_f32_e32 v229, v103, v229
	v_add_f32_e32 v229, v104, v229
	s_waitcnt lgkmcnt(11)
	v_mfma_f32_32x32x16_bf16 v[130:145], v[8:11], v[150:153], v[130:145]
	v_add_f32_e32 v229, v105, v229
	v_add_f32_e32 v229, v106, v229
	v_add_f32_e32 v229, v107, v229
	v_add_f32_e32 v229, v108, v229
	v_add_f32_e32 v229, v109, v229
	v_add_f32_e32 v229, v110, v229
	s_waitcnt lgkmcnt(10)
	v_mfma_f32_32x32x16_bf16 v[114:129], v[174:177], v[150:153], v[114:129]
	v_add_f32_e32 v229, v111, v229
	v_add_f32_e32 v229, v112, v229
	v_add_f32_e32 v228, v113, v229
	s_add_i32 s36, s35, -1
	s_cmp_lt_u32 s36, s30
	s_cselect_b32 s0, 0, s30
	s_cselect_b32 s1, s29, s34
	s_lshl_b32 s0, s0, 6
	s_sub_i32 s37, s1, s0
	s_lshl_b32 s1, s36, 6
	s_add_i32 s37, s37, s1
	s_lshl_b32 s0, s37, 6
	s_add_u32 s48, s44, s0
	s_addc_u32 s49, s45, 0
	s_lshl_b32 s0, s37, 11
	s_add_u32 s46, s42, s0
	s_addc_u32 s47, s43, 0
	global_load_dwordx4 v[174:177], v226, s[48:49]
	s_waitcnt lgkmcnt(9)
	v_mfma_f32_32x32x16_bf16 v[130:145], v[246:249], v[146:149], v[130:145]
	v_cvt_pk_bf16_f32 v70, v98, v99
	v_cvt_pk_bf16_f32 v71, v100, v101
	v_cvt_pk_bf16_f32 v72, v102, v103
	v_cvt_pk_bf16_f32 v73, v104, v105
	global_load_dwordx4 v[8:11], v225, s[46:47]
	global_load_dwordx4 v[4:7], v225, s[46:47] offset:128
	s_waitcnt lgkmcnt(8)
	v_mfma_f32_32x32x16_bf16 v[114:129], v[250:253], v[146:149], v[114:129]
	v_cvt_pk_bf16_f32 v12, v106, v107
	v_cvt_pk_bf16_f32 v13, v108, v109
	v_cvt_pk_bf16_f32 v14, v110, v111
	v_cvt_pk_bf16_f32 v15, v112, v113
	ds_read_b64_tr_b16 v[78:79], v213 offset:20992
	ds_read_b64_tr_b16 v[80:81], v213 offset:22016
	ds_read_b64_tr_b16 v[98:99], v213 offset:23040
	ds_read_b64_tr_b16 v[100:101], v213 offset:24064
	ds_read_b64_tr_b16 v[102:103], v213 offset:25088
	ds_read_b64_tr_b16 v[104:105], v213 offset:26112
	ds_read_b64_tr_b16 v[110:111], v213 offset:27136
	ds_read_b64_tr_b16 v[112:113], v213 offset:28160
	v_max3_f32 v2, v130, v131, v132
	v_max3_f32 v2, v2, v133, v134
	v_max3_f32 v2, v2, v135, v136
	v_max3_f32 v2, v2, v137, v138
	v_max3_f32 v2, v2, v139, v140
	v_max3_f32 v2, v2, v141, v142
	v_max3_f32 v2, v2, v143, v144
	v_max3_f32 v2, v2, v145, v114
	v_max3_f32 v2, v2, v115, v116
	s_waitcnt lgkmcnt(8)
	v_mfma_f32_32x32x16_bf16 v[50:65], v[230:233], v[74:77], v[50:65]
	v_max3_f32 v2, v2, v117, v118
	v_max3_f32 v2, v2, v119, v120
	v_max3_f32 v2, v2, v121, v122
	v_mfma_f32_32x32x16_bf16 v[50:65], v[234:237], v[66:69], v[50:65]
	v_max3_f32 v2, v2, v123, v124
	v_max3_f32 v2, v2, v125, v126
	v_max3_f32 v2, v2, v127, v128
	v_mfma_f32_32x32x16_bf16 v[50:65], v[238:241], v[70:73], v[50:65]
	v_max_f32_e32 v2, v2, v129
	v_mfma_f32_32x32x16_bf16 v[50:65], v[242:245], v[12:15], v[50:65]
	v_cmp_ge_f32_e32 vcc, s28, v2
	s_cmp_eq_u64 vcc, exec
	s_cbranch_scc0 .LBB0_542_2
	v_mov_b32_e32 v2, 1.0

; __device__ __forceinline__ void finishSM(f32x16& p0, f32x16& p1, float alpha, float& l_reg, bf16x8& pa0, bf16x8& pa1, bf16x8& pa2, bf16x8& pa3) {
; #pragma unroll
;     for (int r = 0; r < 16; ++r) p1[r] = EXP_PROBE ? fmaf(p1[r], 0.001f, 1.f) : __builtin_amdgcn_exp2f(p1[r]);
;     float ps = 0.f;
; #pragma unroll
;     for (int r = 0; r < 16; ++r) ps += p0[r];
; #pragma unroll
;     for (int r = 0; r < 16; ++r) ps += p1[r];
;     { auto rr = __builtin_amdgcn_permlane32_swap(__float_as_uint(ps), __float_as_uint(ps), false, false);
;       ps = __uint_as_float(rr[0]) + __uint_as_float(rr[1]); }
;     l_reg = l_reg * alpha + ps;
;     ATT_PKN(p0, 0, pa0); ATT_PKN(p0, 8, pa1); ATT_PKN(p1, 0, pa2); ATT_PKN(p1, 8, pa3);
; }
; template <int DQK> __device__ __forceinline__ void qkt(f32x16& p0, f32x16& p1, const LAS char* buf, const bf16x8* qr, int r32, int hi, const f32x16& negm) {
; #pragma unroll
;     for (int d0 = 0; d0 < 4; ++d0) { const int ch = d0 * 2 + hi;
;         const bf16x8 b0 = *(const LAS bf16x8*)(buf + B_KN + swz64(r32, ch));
;         const bf16x8 b1 = *(const LAS bf16x8*)(buf + B_KN + swz64(32 + r32, ch));
;         p0 = __builtin_amdgcn_mfma_f32_32x32x16_bf16(b0, qr[d0], d0 == 0 ? negm : p0, 0, 0, 0);
;         p1 = __builtin_amdgcn_mfma_f32_32x32x16_bf16(b1, qr[d0], d0 == 0 ? negm : p1, 0, 0, 0); }
;     if constexpr (DQK == 96) {
; #pragma unroll
;         for (int d0 = 0; d0 < 2; ++d0) { const int ch = d0 * 2 + hi;
;             const bf16x8 b0 = *(const LAS bf16x8*)(buf + B_KR + swz32(r32, ch));
;             const bf16x8 b1 = *(const LAS bf16x8*)(buf + B_KR + swz32(32 + r32, ch));
;             p0 = __builtin_amdgcn_mfma_f32_32x32x16_bf16(b0, qr[4 + d0], p0, 0, 0, 0);
;             p1 = __builtin_amdgcn_mfma_f32_32x32x16_bf16(b1, qr[4 + d0], p1, 0, 0, 0); }
;     }
; }
; template <int D0> __device__ __forceinline__ void pv_one(f32x16& od, unsigned vb, bf16x8 pa0, bf16x8 pa1, bf16x8 pa2, bf16x8 pa3) {
;     const s16x4 l0 = tr_read<v_rd_off(D0, 0, 0)>(vb), h0 = tr_read<v_rd_off(D0, 0, 1)>(vb), l1 = tr_read<v_rd_off(D0, 1, 0)>(vb), h1 = tr_read<v_rd_off(D0, 1, 1)>(vb);
;     const s16x4 l2 = tr_read<v_rd_off(D0, 2, 0)>(vb), h2 = tr_read<v_rd_off(D0, 2, 1)>(vb), l3 = tr_read<v_rd_off(D0, 3, 0)>(vb), h3 = tr_read<v_rd_off(D0, 3, 1)>(vb);
;     asm volatile("s_waitcnt lgkmcnt(0)" ::: "memory"); SBAR();
.LBB0_531_2:
	s_waitcnt lgkmcnt(0)
	s_barrier
	ds_read_b128 v[178:181], v209 offset:0
	ds_read_b128 v[182:185], v209 offset:4096
	ds_read_b128 v[170:173], v210 offset:0
	ds_read_b128 v[66:69], v210 offset:4096
	ds_read_b128 v[70:73], v211 offset:0
	ds_read_b128 v[74:77], v211 offset:4096
	ds_read_b128 v[78:81], v212 offset:0
	v_exp_f32_e32 v114, v114
	v_exp_f32_e32 v115, v115
	v_exp_f32_e32 v116, v116
	v_exp_f32_e32 v117, v117
	v_exp_f32_e32 v118, v118
	v_exp_f32_e32 v119, v119
	v_exp_f32_e32 v120, v120
	v_exp_f32_e32 v121, v121
	s_waitcnt lgkmcnt(6)
	v_mfma_f32_32x32x16_bf16 v[130:145], v[178:181], v[166:169], v[82:97]
	ds_read_b128 v[178:181], v212 offset:4096
	v_exp_f32_e32 v122, v122
	v_exp_f32_e32 v123, v123
	v_exp_f32_e32 v124, v124
	v_cvt_pk_bf16_f32 v12, v16, v234
	s_waitcnt lgkmcnt(6)
	v_mfma_f32_32x32x16_bf16 v[98:113], v[182:185], v[166:169], v[82:97]
	ds_read_b128 v[182:185], v219 offset:8192
	v_exp_f32_e32 v125, v125
	v_exp_f32_e32 v126, v126
	v_exp_f32_e32 v127, v127
	v_cvt_pk_bf16_f32 v13, v235, v236
	s_waitcnt lgkmcnt(6)
	v_mfma_f32_32x32x16_bf16 v[130:145], v[170:173], v[162:165], v[130:145]
	ds_read_b128 v[170:173], v219 offset:10240
	v_exp_f32_e32 v128, v128
	v_exp_f32_e32 v129, v129
	v_cvt_pk_bf16_f32 v14, v237, v238
	v_cvt_pk_bf16_f32 v15, v239, v240
	v_add_f32_e32 v252, v16, v234
	v_add_f32_e32 v252, v235, v252
	s_waitcnt lgkmcnt(6)
	v_mfma_f32_32x32x16_bf16 v[98:113], v[66:69], v[162:165], v[98:113]
	ds_read_b128 v[66:69], v220 offset:8192
	v_cvt_pk_bf16_f32 v230, v241, v242
	v_cvt_pk_bf16_f32 v231, v243, v244
	v_add_f32_e32 v252, v236, v252
	v_add_f32_e32 v252, v237, v252
	v_add_f32_e32 v252, v238, v252
	v_add_f32_e32 v252, v239, v252
	s_waitcnt lgkmcnt(6)
	v_mfma_f32_32x32x16_bf16 v[130:145], v[70:73], v[158:161], v[130:145]
	ds_read_b128 v[70:73], v220 offset:10240
	v_cvt_pk_bf16_f32 v232, v245, v246
	v_cvt_pk_bf16_f32 v233, v247, v248
	v_add_f32_e32 v252, v240, v252
	v_add_f32_e32 v252, v241, v252
	v_add_f32_e32 v252, v242, v252
	v_add_f32_e32 v252, v243, v252
	s_waitcnt lgkmcnt(6)
	v_mfma_f32_32x32x16_bf16 v[98:113], v[74:77], v[158:161], v[98:113]
	v_add_f32_e32 v252, v244, v252
	v_add_f32_e32 v252, v245, v252
	v_add_f32_e32 v252, v246, v252
	v_add_f32_e32 v252, v247, v252
	v_add_f32_e32 v252, v248, v252
	v_add_f32_e32 v252, v114, v252
	s_waitcnt lgkmcnt(5)
	v_mfma_f32_32x32x16_bf16 v[130:145], v[78:81], v[154:157], v[130:145]
	ds_read_b64_tr_b16 v[234:235], v213 offset:40960
	ds_read_b64_tr_b16 v[236:237], v213 offset:41984
	ds_read_b64_tr_b16 v[238:239], v213 offset:43008
	ds_read_b64_tr_b16 v[240:241], v213 offset:44032
	v_add_f32_e32 v252, v115, v252
	v_add_f32_e32 v252, v116, v252
	v_add_f32_e32 v252, v117, v252
	s_waitcnt lgkmcnt(8)
	v_mfma_f32_32x32x16_bf16 v[98:113], v[178:181], v[154:157], v[98:113]
	ds_read_b64_tr_b16 v[242:243], v213 offset:45056
	ds_read_b64_tr_b16 v[244:245], v213 offset:46080
	ds_read_b64_tr_b16 v[246:247], v213 offset:47104
	ds_read_b64_tr_b16 v[248:249], v213 offset:48128
	v_add_f32_e32 v252, v118, v252
	v_add_f32_e32 v252, v119, v252
	v_add_f32_e32 v252, v120, v252
	s_waitcnt lgkmcnt(11)
	v_mfma_f32_32x32x16_bf16 v[130:145], v[182:185], v[150:153], v[130:145]
	v_add_f32_e32 v252, v121, v252
	v_add_f32_e32 v252, v122, v252
	v_add_f32_e32 v252, v123, v252
	v_add_f32_e32 v252, v124, v252
	v_add_f32_e32 v252, v125, v252
	v_add_f32_e32 v252, v126, v252
	s_waitcnt lgkmcnt(10)
	v_mfma_f32_32x32x16_bf16 v[98:113], v[170:173], v[150:153], v[98:113]
	v_add_f32_e32 v252, v127, v252
	v_add_f32_e32 v252, v128, v252
	s_waitcnt lgkmcnt(9)
	v_mfma_f32_32x32x16_bf16 v[130:145], v[66:69], v[146:149], v[130:145]
	v_cvt_pk_bf16_f32 v114, v114, v115
	v_cvt_pk_bf16_f32 v115, v116, v117
	v_cvt_pk_bf16_f32 v116, v118, v119
	v_cvt_pk_bf16_f32 v117, v120, v121
	s_cmp_ge_u32 s35, s31
	s_cbranch_scc1 .Lmla_b_noload_2
	s_cmp_lt_u32 s35, s30
	s_cselect_b32 s0, 0, s30
	s_cselect_b32 s1, s29, s34
	s_lshl_b32 s0, s0, 6
	s_sub_i32 s37, s1, s0
	s_lshl_b32 s1, s35, 6
	s_add_i32 s37, s37, s1
	s_lshl_b32 s0, s37, 6
	s_add_u32 s48, s44, s0
	s_addc_u32 s49, s45, 0
	s_lshl_b32 s0, s37, 11
	s_add_u32 s46, s42, s0
	s_addc_u32 s47, s43, 0
	global_load_dwordx4 v[170:173], v226, s[48:49]
	global_load_dwordx4 v[178:181], v225, s[46:47]
	global_load_dwordx4 v[182:185], v225, s[46:47] offset:128
.Lmla_b_ld_done_2:
	s_waitcnt lgkmcnt(8)
	v_mfma_f32_32x32x16_bf16 v[98:113], v[70:73], v[146:149], v[98:113]
	v_cvt_pk_bf16_f32 v118, v122, v123
	v_cvt_pk_bf16_f32 v119, v124, v125
	v_cvt_pk_bf16_f32 v120, v126, v127
	v_cvt_pk_bf16_f32 v121, v128, v129
	v_add_f32_e32 v126, v129, v252
	ds_read_b64_tr_b16 v[66:67], v213 offset:41472
	ds_read_b64_tr_b16 v[68:69], v213 offset:42496
	ds_read_b64_tr_b16 v[70:71], v213 offset:43520
	ds_read_b64_tr_b16 v[72:73], v213 offset:44544
	ds_read_b64_tr_b16 v[74:75], v213 offset:45568
	ds_read_b64_tr_b16 v[76:77], v213 offset:46592
	ds_read_b64_tr_b16 v[78:79], v213 offset:47616
	ds_read_b64_tr_b16 v[80:81], v213 offset:48640
	v_max3_f32 v250, v130, v131, v132
	v_max3_f32 v250, v250, v133, v134
	v_max3_f32 v250, v250, v135, v136
	v_max3_f32 v250, v250, v137, v138
	v_max3_f32 v250, v250, v139, v140
	v_max3_f32 v250, v250, v141, v142
	v_max3_f32 v250, v250, v143, v144
	v_max3_f32 v250, v250, v145, v98
	v_max3_f32 v250, v250, v99, v100
	s_waitcnt lgkmcnt(8)
	v_mfma_f32_32x32x16_bf16 v[50:65], v[234:237], v[12:15], v[50:65]
	v_max3_f32 v250, v250, v101, v102
	v_max3_f32 v250, v250, v103, v104
	v_max3_f32 v250, v250, v105, v106
	v_mfma_f32_32x32x16_bf16 v[50:65], v[238:241], v[230:233], v[50:65]
	v_max3_f32 v250, v250, v107, v108
	v_max3_f32 v250, v250, v109, v110
	v_max3_f32 v250, v250, v111, v112
	v_mfma_f32_32x32x16_bf16 v[50:65], v[242:245], v[114:117], v[50:65]
	v_max_f32_e32 v250, v250, v113
	v_mfma_f32_32x32x16_bf16 v[50:65], v[246:249], v[118:121], v[50:65]
	v_cmp_ge_f32_e32 vcc, s28, v250
	s_cmp_eq_u64 vcc, exec
	v_mov_b32_e32 v16, 1.0
	s_cbranch_scc0 .LBB0_543_2

; #define SBAR() __builtin_amdgcn_sched_barrier(0)
; #define SLOAD(i, j) do { const int _row = KROW(j); skn[i] = *(const bf16x8*)(Knp + (size_t)(_row + sr) * ldk + c8 * 8); sv[i] = *(const bf16x8*)(Vp + (size_t)(_row + sr) * ldv + c8 * 8); \
;         if (krw) skr[i] = *(const bf16x8*)(Krp + (size_t)(_row + sr2) * 32 + c4 * 8); } while (0)
; #define SWRITEO(boff, i) do { *(LAS bf16x8*)(lds + (boff) + kn_st) = skn[i]; *(LAS bf16x8*)(lds + (boff) + v_stw) = sv[i]; if (krw) *(LAS bf16x8*)(lds + (boff) + kr_st) = skr[i]; } while (0)
; #define PVO(boff) do { pv_one<0>(o0, vb0 + (boff), pa0, pa1, pa2, pa3); pv_one<1>(o1, vb0 + (boff), pa0, pa1, pa2, pa3); } while (0)
; #define SWAIT() asm volatile("s_waitcnt vmcnt(2)" ::: "memory")
; #define RESC(a) do { if (__any((a) < 1.f)) { _Pragma("unroll") for (int r = 0; r < 16; ++r) { o0[r] *= (a); o1[r] *= (a); } } } while (0)
; #define ROT() do { const int _t = bV; bV = bK; bK = bW; bW = _t; } while (0)
; __device__ __forceinline__ void finishSM(f32x16& p0, f32x16& p1, float alpha, float& l_reg, bf16x8& pa0, bf16x8& pa1, bf16x8& pa2, bf16x8& pa3) {
;     ...
;     l_reg = l_reg * alpha + ps;
; template <int DQK, bool FIXM> ...
;     ...
;     for (int j = 1; j + 1 < NT; j += 2) {
;         if (!NOBAR_PROBE) __syncthreads();
;         SBAR(); qkt<DQK>(pB0, pB1, lds + bK, qr, r32, hi, negm);
;         finishSM(pA0, pA1, alA, l_reg, pa0, pa1, pa2, pa3); SBAR();
;         SLOAD(1, j + 2); SBAR();
;         if constexpr (FIXM) pv_psm<true>(o0, o1, vb0 + bV, pa0, pa1, pa2, pa3, pB0, pB1, m_reg, negm, alB); else { PVO(bV); partialSM<false>(pB0, pB1, m_reg, negm, alB); }
;         SWAIT(); SWRITEO(bW, 0);
;         if (!FIXM) RESC(alB); ROT();
;         if (!NOBAR_PROBE) __syncthreads();
;         SBAR(); qkt<DQK>(pA0, pA1, lds + bK, qr, r32, hi, negm);
;         finishSM(pB0, pB1, alB, l_reg, pa0, pa1, pa2, pa3); SBAR();
;         if (j + 3 < NT) SLOAD(0, j + 3); SBAR();
;         if constexpr (FIXM) pv_psm<true>(o0, o1, vb0 + bV, pa0, pa1, pa2, pa3, pA0, pA1, m_reg, negm, alA); else { PVO(bV); partialSM<false>(pA0, pA1, m_reg, negm, alA); }
;         SWAIT(); SWRITEO(bW, 1);
;         if (!FIXM) RESC(alA); ROT();
;     }
.LBB0_540_2:
	v_fmac_f32_e32 v228, v227, v223
	s_add_i32 s35, s35, 2
	v_fma_f32 v223, v228, v2, v126
	s_cmp_ge_u32 s36, s12
	s_cbranch_scc1 .Lmla_exit_2
	v_mov_b32_e32 v227, v16
	s_branch .LBB0_523

; #define SBAR() __builtin_amdgcn_sched_barrier(0)
; #define PVO(boff) do { pv_one<0>(o0, vb0 + (boff), pa0, pa1, pa2, pa3); pv_one<1>(o1, vb0 + (boff), pa0, pa1, pa2, pa3); } while (0)
; #define RESC(a) do { if (__any((a) < 1.f)) { _Pragma("unroll") for (int r = 0; r < 16; ++r) { o0[r] *= (a); o1[r] *= (a); } } } while (0)
; __device__ __forceinline__ void finishSM(f32x16& p0, f32x16& p1, float alpha, float& l_reg, bf16x8& pa0, bf16x8& pa1, bf16x8& pa2, bf16x8& pa3) {
;     ...
;     { auto rr = __builtin_amdgcn_permlane32_swap(__float_as_uint(ps), __float_as_uint(ps), false, false);
;       ps = __uint_as_float(rr[0]) + __uint_as_float(rr[1]); }
;     l_reg = l_reg * alpha + ps;
; template <int DQK, bool FIXM> ...
;     ...
;     __syncthreads();
;     SBAR(); qkt<DQK>(pB0, pB1, lds + bK, qr, r32, hi, negm);
;     finishSM(pA0, pA1, alA, l_reg, pa0, pa1, pa2, pa3); SBAR();
;     if constexpr (FIXM) pv_psm<true>(o0, o1, vb0 + bV, pa0, pa1, pa2, pa3, pB0, pB1, m_reg, negm, alB); else { PVO(bV); partialSM<false>(pB0, pB1, m_reg, negm, alB); }
;     if (!FIXM) RESC(alB);
;     finishSM(pB0, pB1, alB, l_reg, pa0, pa1, pa2, pa3); SBAR();
;     PVO(bK);
.Lmla_exit:
	v_sub_u32_e32 v209, v209, v201
	v_sub_u32_e32 v210, v210, v201
	v_sub_u32_e32 v211, v211, v201
	v_sub_u32_e32 v212, v212, v201
	v_sub_u32_e32 v219, v219, v217
	v_sub_u32_e32 v220, v220, v217
	v_mov_b32_e32 v4, v223
	s_nop 1
	v_permlane32_swap_b32_e32 v223, v4
	v_add_f32_e32 v223, v223, v4
	v_add_u32_e32 v17, s11, v213
	v_mov_b64_e32 v[66:67], v[82:83]
	v_mov_b64_e32 v[68:69], v[84:85]
	v_mov_b64_e32 v[70:71], v[86:87]
	v_mov_b64_e32 v[72:73], v[88:89]
	v_mov_b64_e32 v[74:75], v[90:91]
	v_mov_b64_e32 v[76:77], v[92:93]
	v_mov_b64_e32 v[78:79], v[94:95]
	v_mov_b64_e32 v[80:81], v[96:97]
	s_branch .LBB0_544
